# sel block head: the has-tile path falls through (no-tile DMA code moved out of line)
# speedup vs baseline: 1.0034x; 1.0034x over previous
; #define LAS __attribute__((address_space(3)))
; __device__ __forceinline__ unsigned lds_addr(const LAS void* p) { return (unsigned)(size_t)p; }
; __device__ __forceinline__ void ringS_dma(const RingSLane& R, const char* K8p, const char* VTp, LAS unsigned char* sb, int wave) {
;     __builtin_amdgcn_global_load_lds((const unsigned*)(K8p + R.so[0]), (LAS unsigned*)(sb + wave * 1024), 16, 0, 0);
;     __builtin_amdgcn_global_load_lds((const unsigned*)((wave == 0 ? K8p : VTp) + R.so[1]), (LAS unsigned*)(sb + (wave + 8) * 1024), 16, 0, 0);
;     if (wave <= 2) __builtin_amdgcn_global_load_lds((const unsigned*)(VTp + R.so[2]), (LAS unsigned*)(sb + (wave + 16) * 1024), 16, 0, 0);
; }
; template <bool DUMMY> __device__ __forceinline__ void sel_phase(Frame& F) {
;     ...
;                 if (h > 0 && ((cj >> (23 + h)) & 1u) == 0u) continue;
;                 const int jc = (int)((cj >> (8 * h)) & 0xffu);
;                 LAS unsigned char* sb = F.lds + (((p & 1) * 3) + h) * SLOTS;
;                 unsigned byte = (cb >> (8 * h)) & 0xffu;
;                 if (DUMMY && MK_EXP == 1) byte = 0u;
;                 const unsigned a0 = byte & 0xfu, a1 = byte >> 4;
;                 if (byte == 0u) continue;
;                 const bool selA = ((a0 >> (c >> 2)) & 1u) != 0u, selB = ((a1 >> (c >> 2)) & 1u) != 0u;
;                 const float NINF = -__builtin_inff();
;                 const int kb = jc * 64; const bool diag = (jc == cur); f32x4 s0[4], s1[4];
;                 const float bA = selA ? 0.f : NINF, bB = selB ? 0.f : NINF;
;                 if (a0 != 0u) {
;                     const float rf = sm8_ref(g0);
;                     VT8Frag vf; qk8_tile_c(s0, g0, lds_addr(sb) + (unsigned)klane, bA + (5.f - rf)); pv8_issue(vf, lds_addr(sb + K8TB) + (unsigned)vtlane);
.LBB0_1799:
	s_lshr_b32 s45, s67, s36
	s_and_b32 s97, s45, 0xff
	s_cbranch_scc0 .Lsel_notile
	ds_read_b128 v[84:87], v208 offset:0
	ds_read_b128 v[88:91], v208 offset:16
	ds_read_b128 v[92:95], v208 offset:0x900
	ds_read_b128 v[96:99], v208 offset:0x910
	ds_read_b128 v[118:121], v208 offset:0x1200
	ds_read_b128 v[122:125], v208 offset:0x1210
	s_bitcmp1_b32 s99, s37
	s_cbranch_scc0 .Lsel_tile2
	s_lshr_b32 vcc_lo, s60, s36
	s_and_b32 vcc_lo, vcc_lo, 0xff
	s_lshl_b32 vcc_lo, vcc_lo, 13
	s_add_u32 s12, s62, vcc_lo
	s_addc_u32 s13, s63, 0
	s_add_u32 s100, s64, vcc_lo
	s_addc_u32 s101, s65, 0
	s_mul_i32 vcc_hi, s37, 0x4c00
	s_add_i32 vcc_hi, s98, vcc_hi
	s_mov_b32 m0, vcc_hi
	s_cmp_lg_u64 s[16:17], 0
	global_load_lds_dwordx4 v102, s[12:13]
	s_cselect_b32 s13, s13, s101
	s_cselect_b32 s12, s12, s100
	s_add_i32 m0, vcc_hi, 0x2000
	s_cmp_lg_u64 s[10:11], 0
	global_load_lds_dwordx4 v106, s[12:13]
	s_cbranch_scc1 .Lsel_tile2
	s_add_i32 m0, vcc_hi, 0x4000
	s_nop 0
	global_load_lds_dwordx4 v108, s[100:101]

; #define LAS __attribute__((address_space(3)))
; __device__ __forceinline__ void ringS_dma(const RingSLane& R, const char* K8p, const char* VTp, LAS unsigned char* sb, int wave) {
;     __builtin_amdgcn_global_load_lds((const unsigned*)(K8p + R.so[0]), (LAS unsigned*)(sb + wave * 1024), 16, 0, 0);
;     __builtin_amdgcn_global_load_lds((const unsigned*)((wave == 0 ? K8p : VTp) + R.so[1]), (LAS unsigned*)(sb + (wave + 8) * 1024), 16, 0, 0);
;     if (wave <= 2) __builtin_amdgcn_global_load_lds((const unsigned*)(VTp + R.so[2]), (LAS unsigned*)(sb + (wave + 16) * 1024), 16, 0, 0);
; }
.Lsel_notile:
	s_bitcmp1_b32 s99, s37
	s_cbranch_scc0 .LBB0_1798
	s_lshr_b32 s12, s60, s36
	s_and_b32 s12, s12, 0xff
	s_lshl_b32 s12, s12, 13
	s_add_u32 s44, s62, s12
	s_addc_u32 s45, s63, 0
	s_add_u32 s12, s64, s12
	s_addc_u32 s13, s65, 0
	s_mul_i32 s97, s37, 0x4c00
	s_add_i32 s97, s98, s97
	s_mov_b32 m0, s97
	s_and_b64 vcc, exec, s[16:17]
	global_load_lds_dwordx4 v102, s[44:45]
	s_cselect_b32 s45, s45, s13
	s_cselect_b32 s44, s44, s12
	s_add_i32 m0, s97, 0x2000
	s_and_b64 vcc, exec, s[10:11]
	global_load_lds_dwordx4 v106, s[44:45]
	s_cbranch_vccnz .LBB0_1798
	s_add_i32 m0, s97, 0x4000
	s_nop 0
	global_load_lds_dwordx4 v108, s[12:13]
	s_branch .LBB0_1798
